# router chunks assigned by XCD (each workgroup routes tokens of row panels its own XCD produced), so the rec-out to router seam also releases per XCD: four per-XCD seams
# baseline (speedup 1.0000x reference)
; __device__ __forceinline__ unsigned xb_add(unsigned* p, unsigned v) { return __hip_atomic_fetch_add(p, v, __ATOMIC_RELAXED, __HIP_MEMORY_SCOPE_AGENT); }
; __device__ __forceinline__ void xcd_barrier(const XcdBarrier& b) {
;     ...
;             __builtin_amdgcn_fence(__ATOMIC_ACQUIRE, "agent");
;             xb_add(&bar[XB_XGEN(b.x)], 1u);
;             asm volatile("s_waitcnt vmcnt(0)" ::: "memory");
.Lxcdlocal_3:
	s_mov_b64 s[6:7], exec
	v_mbcnt_lo_u32_b32 v0, s6, 0
	v_mbcnt_hi_u32_b32 v0, s7, v0
	v_cmp_eq_u32_e32 vcc, 0, v0
	s_waitcnt vmcnt(0)
	buffer_inv sc1
	s_and_saveexec_b64 s[8:9], vcc
	s_cbranch_execz .LBB0_1809
	s_bcnt1_i32_b64 s6, s[6:7]
	v_mov_b32_e32 v0, 0x2000
	v_mov_b32_e32 v1, s6
	global_atomic_add v0, v1, s[4:5] offset:1024

; #define LAS __attribute__((address_space(3)))
; __global__ void __launch_bounds__(NTHR, 2) fwd_kernel(Args args) {
;     ...
;         LAS float* Rg = (LAS float*)ring;
;         LAS int* lcnt = (LAS int*)lepi;
;         for (int i = tid; i < DM * 8; i += NTHR) { const int k = i >> 3, e = i & 7; Rg[e * DM + k] = od_ffn_norm[k] * od_router[i]; }
;         for (int c = wg; c < T / 64; c += G) {
.LBB0_1812:
	v_readlane_b32 s0, v254, 0
	v_readlane_b32 s1, v254, 1
	s_cmp_lt_i32 s0, 15
	s_cselect_b64 s[0:1], -1, 0
	s_and_b64 s[2:3], s[0:1], s[2:3]
	s_andn2_b64 vcc, exec, s[2:3]
	s_lshl_b32 s33, s85, 3
	s_cbranch_vccnz .LBB0_1851
	v_mbcnt_lo_u32_b32 v210, -1, 0
	v_mbcnt_hi_u32_b32 v210, -1, v210
	s_load_dwordx4 s[4:7], s[94:95], 0xb0
	s_load_dwordx2 s[8:9], s[94:95], 0xe0
	v_add_u32_e32 v211, s91, v210
	v_lshlrev_b32_e32 v208, 4, v210
	v_lshlrev_b32_e32 v212, 5, v211
	v_lshlrev_b32_e32 v213, 2, v211
	v_lshrrev_b32_e32 v214, 3, v211
	v_lshlrev_b32_e32 v214, 4, v214
	v_and_b32_e32 v215, 7, v211
	v_lshl_add_u32 v214, v215, 11, v214
	v_add_u32_e32 v216, 0x4000, v212
	v_add_u32_e32 v217, 0x8000, v212
	v_add_u32_e32 v218, 0xc000, v212
	v_add_u32_e32 v219, 0x1000, v213
	s_waitcnt lgkmcnt(0)
	global_load_dwordx4 v[64:67], v212, s[6:7]
	global_load_dwordx4 v[68:71], v212, s[6:7] offset:16
	global_load_dwordx4 v[72:75], v216, s[6:7]
	global_load_dwordx4 v[76:79], v216, s[6:7] offset:16
	global_load_dwordx4 v[80:83], v217, s[6:7]
	global_load_dwordx4 v[84:87], v217, s[6:7] offset:16
	global_load_dwordx4 v[88:91], v218, s[6:7]
	global_load_dwordx4 v[92:95], v218, s[6:7] offset:16
	global_load_dword v96, v213, s[4:5]
	global_load_dword v97, v213, s[4:5] offset:2048
	global_load_dword v98, v219, s[4:5]
	global_load_dword v99, v219, s[4:5] offset:2048
	s_add_u32 s10, s8, 0x35000000
	s_addc_u32 s11, s9, 0
	s_mov_b32 s15, 0xffff0000
	s_mov_b32 s63, 0xf800000
	s_mov_b32 s65, 0x3fb8aa3b
	s_mov_b32 s66, 0xc2ce8ed0
	s_mov_b32 s67, 0x42b17218
	v_mov_b32_e32 v220, 0
	v_mov_b32_e32 v221, 1
	v_mov_b32_e32 v222, 0x358637bd
	v_mov_b32_e32 v223, 0x260
	v_mov_b32_e32 v224, 0xff800000
	v_mov_b32_e32 v225, 0x7f800000
	v_mov_b32_e32 v226, 0x362000
	v_mov_b32_e32 v227, 0x372000
	v_mov_b32_e32 v228, 0x352000
	s_mov_b32 s20, 0x20000
	v_lshl_add_u32 v229, v211, 2, s20
	s_waitcnt vmcnt(0)
	v_mul_f32_e32 v64, v64, v96
	v_mul_f32_e32 v65, v65, v96
	v_mul_f32_e32 v66, v66, v96
	v_mul_f32_e32 v67, v67, v96
	v_mul_f32_e32 v68, v68, v96
	v_mul_f32_e32 v69, v69, v96
	v_mul_f32_e32 v70, v70, v96
	v_mul_f32_e32 v71, v71, v96
	v_mul_f32_e32 v72, v72, v97
	v_mul_f32_e32 v73, v73, v97
	v_mul_f32_e32 v74, v74, v97
	v_mul_f32_e32 v75, v75, v97
	v_mul_f32_e32 v76, v76, v97
	v_mul_f32_e32 v77, v77, v97
	v_mul_f32_e32 v78, v78, v97
	v_mul_f32_e32 v79, v79, v97
	v_mul_f32_e32 v80, v80, v98
	v_mul_f32_e32 v81, v81, v98
	v_mul_f32_e32 v82, v82, v98
	v_mul_f32_e32 v83, v83, v98
	v_mul_f32_e32 v84, v84, v98
	v_mul_f32_e32 v85, v85, v98
	v_mul_f32_e32 v86, v86, v98
	v_mul_f32_e32 v87, v87, v98
	v_mul_f32_e32 v88, v88, v99
	v_mul_f32_e32 v89, v89, v99
	v_mul_f32_e32 v90, v90, v99
	v_mul_f32_e32 v91, v91, v99
	v_mul_f32_e32 v92, v92, v99
	v_mul_f32_e32 v93, v93, v99
	v_mul_f32_e32 v94, v94, v99
	v_mul_f32_e32 v95, v95, v99
	ds_write_b128 v214, v[64:67] offset:0
	ds_write_b128 v214, v[68:71] offset:1024
	ds_write_b128 v214, v[72:75] offset:16384
	ds_write_b128 v214, v[76:79] offset:17408
	ds_write_b128 v214, v[80:83] offset:32768
	ds_write_b128 v214, v[84:87] offset:33792
	ds_write_b128 v214, v[88:91] offset:49152
	ds_write_b128 v214, v[92:95] offset:50176
	v_readlane_b32 s12, v254, 32
	s_and_b32 s13, s12, 7
	s_lshl_b32 s13, s13, 5
	s_lshr_b32 s12, s12, 3
	s_or_b32 s12, s12, s13
